# speedup vs baseline: 1.0171x; 1.0171x over previous
_Z11attn_kernelPKDF16_S0_S0_PfPDF16_S1_:
	s_lshl_b32 s3, s2, 7
	s_lshr_b32 s4, s2, 2
	s_and_b32 s3, s3, 0x180
	s_and_b32 s4, s4, 0x3ffffffe
	s_add_i32 s3, s3, s4
	s_bfe_u32 s2, s2, 0x10002
	s_or_b32 s40, s3, s2
	s_mov_b32 s41, 0
	s_lshl_b64 s[2:3], s[40:41], 2
	s_getpc_b64 s[4:5]
	s_add_u32 s4, s4, g_tab@rel32@lo+4
	s_addc_u32 s5, s5, g_tab@rel32@hi+12
	s_add_u32 s42, s4, s2
	s_addc_u32 s43, s5, s3
	s_load_dword s12, s[42:43], 0x0
	s_load_dwordx4 s[4:7], s[0:1], 0x8
	s_load_dword s76, s[42:43], 0x1000
	s_load_dwordx2 s[80:81], s[0:1], 0x0
	s_load_dwordx4 s[84:87], s[0:1], 0x18
	s_load_dwordx2 s[88:89], s[0:1], 0x28
	v_lshlrev_b32_e32 v2, 4, v0
	s_movk_i32 s8, 0x70
	v_readfirstlane_b32 s3, v0
	s_waitcnt lgkmcnt(0)
	s_add_u32 s70, s4, 0x2000
	s_addc_u32 s71, s5, 0
	s_add_u32 s72, s6, 0x2000
	s_addc_u32 s73, s7, 0
	s_and_b32 s2, s12, 3
	s_lshl_b32 s10, s2, 19
	v_bitop3_b32 v10, v2, s8, v0 bitop3:0x48
	s_add_u32 s8, s6, s10
	s_addc_u32 s9, s7, 0
	s_lshr_b32 s13, s3, 6
	s_bfe_u32 s40, s12, 0x70007
	s_bfe_u32 s33, s12, 0x6000e
	v_and_b32_e32 v1, 0x1f80, v2
	s_add_u32 s10, s4, s10
	v_or_b32_e32 v50, v10, v1
	v_mov_b32_e32 v51, 0
	s_addc_u32 s11, s5, 0
	v_lshl_add_u64 v[52:53], s[10:11], 0, v[50:51]
	v_lshl_add_u64 v[54:55], s[8:9], 0, v[50:51]
	s_lshl_b32 s8, s40, 13
	s_mov_b32 s9, s41
	s_lshl_b32 s50, s13, 10
	v_lshl_add_u64 v[2:3], v[52:53], 0, s[8:9]
	s_mov_b32 m0, s50
	s_add_i32 s51, s50, 0x2000
	global_load_lds_dwordx4 v[2:3], off
	v_lshl_add_u64 v[2:3], v[54:55], 0, s[8:9]
	s_mov_b32 m0, s51
	s_cmp_eq_u32 s33, 0
	global_load_lds_dwordx4 v[2:3], off
	s_cbranch_scc1 .LBB2_30
	s_mov_b64 s[14:15], s[80:81]
	s_mov_b64 s[8:9], s[84:85]
	s_mov_b64 s[10:11], s[86:87]
	s_mov_b64 s[44:45], s[88:89]
	s_cmp_lt_u32 s13, 4
	s_cbranch_scc1 .Lattn_prio_done
	s_setprio 1
.Lattn_prio_done:
	s_lshl_b32 s52, s13, 4
	s_lshl_b32 s0, s2, 12
	v_and_b32_e32 v56, 15, v0
	v_bfe_u32 v15, v0, 4, 2
	v_lshrrev_b32_e32 v14, 1, v0
	v_bfe_u32 v2, v0, 1, 3
	s_add_i32 s54, s52, s0
	v_lshlrev_b32_e32 v16, 7, v56
	v_bitop3_b32 v3, v15, v14, 7 bitop3:0x78
	v_bitop3_b32 v2, v15, v2, 4 bitop3:0x36
	s_bfe_u32 s53, s12, 0x50002
	v_or_b32_e32 v18, s54, v56
	v_lshl_or_b32 v57, v3, 4, v16
	v_lshl_or_b32 v81, v2, 4, v16
	v_lshl_add_u32 v2, s53, 7, v18
	v_mov_b32_e32 v3, v51
	v_lshlrev_b64 v[2:3], 7, v[2:3]
	v_and_b32_e32 v50, 48, v0
	s_waitcnt lgkmcnt(0)
	v_lshl_add_u64 v[2:3], s[14:15], 0, v[2:3]
	v_lshl_add_u64 v[12:13], v[2:3], 0, v[50:51]
	global_load_dwordx4 v[2:5], v[12:13], off offset:64
	global_load_dwordx4 v[6:9], v[12:13], off
	v_and_b32_e32 v11, 63, v0
	v_bfe_u32 v12, v0, 5, 1
	s_mulk_i32 s13, 0xc00
	v_and_b32_e32 v13, 7, v0
	v_cmp_gt_u32_e64 s[0:1], 16, v11
	v_bitop3_b32 v11, v12, v0, 7 bitop3:0x78
	s_lshr_b32 s55, s3, 8
	s_add_i32 s3, s50, s13
	v_and_b32_e32 v14, 8, v14
	v_lshlrev_b32_e32 v23, 4, v11
	v_bitop3_b32 v11, v12, v13, 2 bitop3:0x36
	v_add3_u32 v19, s3, v16, v14
	v_bfe_u32 v14, v0, 3, 3
	v_lshlrev_b32_e32 v24, 4, v11
	v_bitop3_b32 v11, v12, v13, 4 bitop3:0x36
	v_bitop3_b32 v16, v14, v0, 7 bitop3:0x78
	v_lshlrev_b32_e32 v25, 4, v11
	v_bitop3_b32 v11, v12, v13, 6 bitop3:0x36
	v_bitop3_b32 v0, v15, v0, 15 bitop3:0x78
	v_lshl_add_u64 v[58:59], s[14:15], 0, v[50:51]
	v_lshlrev_b32_e32 v50, 4, v13
	v_lshlrev_b32_e32 v13, 4, v11
	v_or_b32_e32 v11, 8, v14
	v_lshlrev_b32_e32 v86, 4, v0
	v_bitop3_b32 v0, v15, v56, 4 bitop3:0x36
	v_or_b32_e32 v17, 4, v15
	v_lshl_add_u32 v21, v16, 4, s3
	v_lshlrev_b32_e32 v26, 7, v14
	v_lshlrev_b32_e32 v12, 6, v14
	v_lshlrev_b32_e32 v27, 7, v11
	v_lshlrev_b32_e32 v14, 6, v11
	v_lshlrev_b32_e32 v87, 4, v0
	v_or_b32_e32 v0, 8, v15
	v_bitop3_b32 v11, v15, v56, 8 bitop3:0x36
	v_bitop3_b32 v16, v15, v56, 12 bitop3:0x36
	v_lshlrev_b32_e32 v83, 2, v15
	v_add_u32_e32 v84, 0x80, v18
	v_lshl_add_u64 v[60:61], s[10:11], 0, v[50:51]
	v_lshlrev_b32_e32 v50, 4, v56
	v_lshlrev_b32_e32 v88, 4, v11
	v_or_b32_e32 v11, 12, v15
	v_lshlrev_b32_e32 v89, 4, v16
	v_lshl_add_u32 v28, v15, 8, s3
	v_lshlrev_b32_e32 v16, 6, v15
	v_lshl_add_u32 v15, v17, 8, s3
	v_lshlrev_b32_e32 v18, 6, v17
	v_lshl_add_u32 v17, v0, 8, s3
	v_lshlrev_b32_e32 v20, 6, v0
	v_add_u32_e32 v0, v1, v10
	v_lshl_add_u64 v[62:63], s[8:9], 0, v[50:51]
	s_lshl_b32 s8, s53, 1
	v_lshl_or_b32 v50, s2, 19, v0
	v_mov_b32_e32 v76, v50
	s_mov_b64 s[46:47], 0x2000
	v_lshl_add_u32 v85, v56, 8, s3
	v_lshl_add_u32 v29, v11, 8, s3
	v_lshlrev_b32_e32 v22, 6, v11
	s_add_i32 s3, s55, s8
	v_lshl_add_u64 v[10:11], v[50:51], 0, s[46:47]
	v_or_b32_e32 v82, s52, v56
	s_add_i32 s56, s8, 2
	s_sub_i32 s57, 0, s3
	v_lshl_add_u64 v[0:1], s[4:5], 0, v[10:11]
	v_lshl_add_u64 v[64:65], s[6:7], 0, v[10:11]
	s_mov_b32 s58, 0x40c00000
	s_mov_b32 s36, 0x3c003c00
	v_mov_b32_e32 v116, s36
	v_mov_b32_e32 v117, s36
	v_mov_b32_e32 v118, s36
	v_mov_b32_e32 v119, s36
	v_add_u32_e32 v90, v19, v23
	v_add_u32_e32 v91, v19, v24
	v_add_u32_e32 v92, v19, v25
	v_add_u32_e32 v93, v19, v13
	v_add_u32_e32 v94, v21, v26
	v_lshlrev_b32_e32 v50, 1, v12
	v_add_u32_e32 v95, v21, v27
	v_lshlrev_b32_e32 v66, 1, v14
	v_add_u32_e32 v96, v28, v86
	v_lshlrev_b32_e32 v68, 2, v16
	v_add_u32_e32 v97, v15, v87
	v_lshlrev_b32_e32 v70, 2, v18
	v_add_u32_e32 v98, v17, v88
	v_lshlrev_b32_e32 v72, 2, v20
	v_add_u32_e32 v99, v29, v89
	v_lshlrev_b32_e32 v74, 2, v22
	v_mov_b32_e32 v100, 0xff800000
	v_mov_b32_e32 v101, 0xf149f2ca
	s_mov_b32 s59, s41
	s_branch .LBB2_3
